# previous best + s_setprio 1 hoisted above the barrier in the two remaining gate/up and down K-loop blocks (pure move)
# speedup vs baseline: 1.0046x; 1.0046x over previous
; #define G8_STAGE(bufoff, gbase, voff) do { _Pragma("unroll") for (int _i = 0; _i < 2; ++_i) \
;         __builtin_amdgcn_global_load_lds((const unsigned*)((const char*)(gbase) + (voff)[_i]), (LAS unsigned*)(lds + (bufoff) + ldsw + _i * 8192), 16, 0, 0); } while (0)
; #define G8_LDA(dst, b, h) do { _Pragma("unroll") for (int m = 0; m < 4; ++m) _Pragma("unroll") for (int k = 0; k < 2; ++k) dst[m][k] = *(const LAS bf16x8*)(lds + G8_SA(b, h) + aoff + m * 2048 + k * 1024); } while (0)
; #define G8_LDB(dst, b, h) do { _Pragma("unroll") for (int n = 0; n < 2; ++n) _Pragma("unroll") for (int k = 0; k < 2; ++k) dst[n][k] = *(const LAS bf16x8*)(lds + G8_SB(b, h) + boff + n * 2048 + k * 1024); } while (0)
; #define G8_MMA(ai, bj, At, Bt) do { __builtin_amdgcn_s_setprio(1); _Pragma("unroll") for (int m = 0; m < 4; ++m) _Pragma("unroll") for (int n = 0; n < 2; ++n) _Pragma("unroll") for (int k = 0; k < 2; ++k) \
;         acc[ai][bj][m][n] = __builtin_amdgcn_mfma_f32_16x16x32_bf16(Bt[n][k], At[m][k], acc[ai][bj][m][n], 0, 0, 0); __builtin_amdgcn_s_setprio(0); } while (0)
; template <class Epi, class Sched>
; __device__ __forceinline__ void gemm_phase(LAS unsigned char* lds, const int K, const Sched& S, const Epi& E) {
;     ...
;         const bool has_next = S.next(ui + 1, nxt);
;         const char* nA = has_next ? nxt.A : cA; const char* nB = has_next ? nxt.B : cB;
; #pragma unroll 1
;         for (int t = 0; t < nt; t += 2) {
;             const bool last = (t == nt - 2);
;             const char* a1 = cA + (size_t)(t + 1) * kstep;
;             const char* a2 = last ? nA : cA + (size_t)(t + 2) * kstep; const char* b2 = last ? nB : cB + (size_t)(t + 2) * kstep;
;             const char* a3 = a2 + kstep; const char* b3 = b2 + kstep;
;             G8_LDB(B0, 0, 0); G8_SCHED; G8_LDA(At, 0, 0); G8_STAGE(G8_SA(1, 1), a1, oc[1]);
;             if (last && has_next) S.aoff(nxt, tid, oc);
;             G8_WAIT_L(8); G8_BAR; G8_WAIT_L(0); G8_MMA(0, 0, At, B0); G8_BAR; G8_SCHED;
;             G8_LDB(B1, 0, 1); G8_STAGE(G8_SB(0, 0), b2, voffB);
;             G8_BAR; G8_WAIT_L(0); G8_MMA(0, 1, At, B1); G8_BAR;
;             G8_LDA(At, 0, 1); G8_STAGE(G8_SA(0, 0), a2, oc[0]);
;             G8_BAR; G8_WAIT_L(0); G8_MMA(1, 0, At, B0); G8_BAR; G8_SCHED;
;             G8_STAGE(G8_SB(0, 1), b2 + hstep, voffB);
;             G8_WAIT_V(6); G8_BAR; G8_MMA(1, 1, At, B1); G8_BAR;
.LBB0_2526:
	s_add_u32 s34, s22, 0x80
	s_addc_u32 s35, s23, 0
	s_and_b64 s[24:25], s[24:25], exec
	s_cselect_b32 s35, s1, s35
	s_cselect_b32 s34, s0, s34
	s_cselect_b32 s25, s13, s56
	s_cselect_b32 s24, s12, s55
	s_setprio 1
	s_waitcnt lgkmcnt(8)
	s_barrier
	s_waitcnt lgkmcnt(0)
	s_waitcnt lgkmcnt(0)
	v_mfma_f32_16x16x32_bf16 v[126:129], v[130:133], v[170:173], v[126:129]
	v_mfma_f32_16x16x32_bf16 v[122:125], v[138:141], v[170:173], v[122:125]
	v_mfma_f32_16x16x32_bf16 v[110:113], v[130:133], v[162:165], v[110:113]
	v_mfma_f32_16x16x32_bf16 v[106:109], v[138:141], v[162:165], v[106:109]
	v_mfma_f32_16x16x32_bf16 v[94:97], v[130:133], v[154:157], v[94:97]
	v_mfma_f32_16x16x32_bf16 v[90:93], v[138:141], v[154:157], v[90:93]
	v_mfma_f32_16x16x32_bf16 v[78:81], v[130:133], v[146:149], v[78:81]
	v_mfma_f32_16x16x32_bf16 v[74:77], v[138:141], v[146:149], v[74:77]
	v_mfma_f32_16x16x32_bf16 v[126:129], v[134:137], v[174:177], v[126:129]
	v_mfma_f32_16x16x32_bf16 v[122:125], v[142:145], v[174:177], v[122:125]
	v_mfma_f32_16x16x32_bf16 v[110:113], v[134:137], v[166:169], v[110:113]
	v_mfma_f32_16x16x32_bf16 v[106:109], v[142:145], v[166:169], v[106:109]
	v_mfma_f32_16x16x32_bf16 v[94:97], v[134:137], v[158:161], v[94:97]
	v_mfma_f32_16x16x32_bf16 v[90:93], v[142:145], v[158:161], v[90:93]
	v_mfma_f32_16x16x32_bf16 v[78:81], v[134:137], v[150:153], v[78:81]
	v_mfma_f32_16x16x32_bf16 v[74:77], v[142:145], v[150:153], v[74:77]
	s_setprio 0
	s_barrier
	s_add_i32 s60, 0, 0x14000
	s_mov_b32 m0, s43
	v_add_u32_e32 v183, s60, v198
	v_lshl_add_u64 v[232:233], s[24:25], 0, v[178:179]
	ds_read_b128 v[216:219], v183
	ds_read_b128 v[220:223], v183 offset:1024
	ds_read_b128 v[224:227], v183 offset:2048
	ds_read_b128 v[228:231], v183 offset:3072
	global_load_lds_dwordx4 v[232:233], off
	v_lshl_add_u64 v[234:235], s[24:25], 0, v[180:181]
	s_mov_b32 m0, s44
	s_nop 0
	global_load_lds_dwordx4 v[234:235], off
	s_setprio 1
	s_barrier
	s_waitcnt lgkmcnt(0)
	v_mfma_f32_16x16x32_bf16 v[118:121], v[216:219], v[170:173], v[118:121]
	v_mfma_f32_16x16x32_bf16 v[114:117], v[224:227], v[170:173], v[114:117]
	v_mfma_f32_16x16x32_bf16 v[102:105], v[216:219], v[162:165], v[102:105]
	v_mfma_f32_16x16x32_bf16 v[98:101], v[224:227], v[162:165], v[98:101]
	v_mfma_f32_16x16x32_bf16 v[86:89], v[216:219], v[154:157], v[86:89]
	v_mfma_f32_16x16x32_bf16 v[82:85], v[224:227], v[154:157], v[82:85]
	v_mfma_f32_16x16x32_bf16 v[70:73], v[216:219], v[146:149], v[70:73]
	v_mfma_f32_16x16x32_bf16 v[66:69], v[224:227], v[146:149], v[66:69]
	v_mfma_f32_16x16x32_bf16 v[118:121], v[220:223], v[174:177], v[118:121]
	s_mov_b32 m0, s42
	v_mfma_f32_16x16x32_bf16 v[114:117], v[228:231], v[174:177], v[114:117]
	v_mfma_f32_16x16x32_bf16 v[102:105], v[220:223], v[166:169], v[102:105]
	v_mfma_f32_16x16x32_bf16 v[98:101], v[228:231], v[166:169], v[98:101]
	v_mfma_f32_16x16x32_bf16 v[86:89], v[220:223], v[158:161], v[86:89]
	v_mfma_f32_16x16x32_bf16 v[82:85], v[228:231], v[158:161], v[82:85]
	v_mfma_f32_16x16x32_bf16 v[70:73], v[220:223], v[150:153], v[70:73]
	v_mfma_f32_16x16x32_bf16 v[66:69], v[228:231], v[150:153], v[66:69]
	s_setprio 0
	s_barrier
	ds_read_b128 v[146:149], v200 offset:16384
	ds_read_b128 v[150:153], v200 offset:17408
	ds_read_b128 v[154:157], v200 offset:18432
	ds_read_b128 v[158:161], v200 offset:19456
	ds_read_b128 v[162:165], v200 offset:20480
	ds_read_b128 v[166:169], v200 offset:21504
	ds_read_b128 v[170:173], v200 offset:22528
	ds_read_b128 v[174:177], v200 offset:23552
	global_load_lds_dwordx4 v0, s[34:35]
	s_mov_b32 m0, s45
	v_mov_b32_e32 v183, v1
	global_load_lds_dwordx4 v182, s[34:35]
	s_setprio 1
	s_barrier
	s_waitcnt lgkmcnt(0)
	v_lshl_add_u64 v[236:237], s[34:35], 0, v[0:1]
	v_lshl_add_u64 v[238:239], s[34:35], 0, v[182:183]
	s_waitcnt lgkmcnt(0)
	v_mfma_f32_16x16x32_bf16 v[62:65], v[130:133], v[146:149], v[62:65]
	v_mfma_f32_16x16x32_bf16 v[58:61], v[138:141], v[146:149], v[58:61]
	v_mfma_f32_16x16x32_bf16 v[46:49], v[130:133], v[154:157], v[46:49]
	v_mfma_f32_16x16x32_bf16 v[42:45], v[138:141], v[154:157], v[42:45]
	v_mfma_f32_16x16x32_bf16 v[30:33], v[130:133], v[162:165], v[30:33]
	v_mfma_f32_16x16x32_bf16 v[26:29], v[138:141], v[162:165], v[26:29]
	v_mfma_f32_16x16x32_bf16 v[14:17], v[130:133], v[170:173], v[14:17]
	v_mfma_f32_16x16x32_bf16 v[10:13], v[138:141], v[170:173], v[10:13]
	v_mfma_f32_16x16x32_bf16 v[62:65], v[134:137], v[150:153], v[62:65]
	v_mfma_f32_16x16x32_bf16 v[58:61], v[142:145], v[150:153], v[58:61]
	v_mfma_f32_16x16x32_bf16 v[46:49], v[134:137], v[158:161], v[46:49]
	v_mfma_f32_16x16x32_bf16 v[42:45], v[142:145], v[158:161], v[42:45]
	v_mfma_f32_16x16x32_bf16 v[30:33], v[134:137], v[166:169], v[30:33]
	v_mfma_f32_16x16x32_bf16 v[26:29], v[142:145], v[166:169], v[26:29]
	v_mfma_f32_16x16x32_bf16 v[14:17], v[134:137], v[174:177], v[14:17]
	v_mfma_f32_16x16x32_bf16 v[10:13], v[142:145], v[174:177], v[10:13]
	s_setprio 0
	s_barrier
	s_add_u32 s58, s24, 0x40000
	s_addc_u32 s59, s25, 0
	s_add_i32 s60, s60, s41
	v_lshl_add_u64 v[130:131], s[58:59], 0, v[178:179]
	s_mov_b32 m0, s60
	s_nop 0
	global_load_lds_dwordx4 v[130:131], off
	v_lshl_add_u64 v[130:131], s[58:59], 0, v[180:181]
	s_add_i32 m0, s60, 0x2000
	s_nop 0
	global_load_lds_dwordx4 v[130:131], off
	s_waitcnt vmcnt(6)
	s_setprio 1
	s_barrier
; #define G8_STAGE(bufoff, gbase, voff) do { _Pragma("unroll") for (int _i = 0; _i < 2; ++_i) \
;         __builtin_amdgcn_global_load_lds((const unsigned*)((const char*)(gbase) + (voff)[_i]), (LAS unsigned*)(lds + (bufoff) + ldsw + _i * 8192), 16, 0, 0); } while (0)
; #define G8_LDA(dst, b, h) do { _Pragma("unroll") for (int m = 0; m < 4; ++m) _Pragma("unroll") for (int k = 0; k < 2; ++k) dst[m][k] = *(const LAS bf16x8*)(lds + G8_SA(b, h) + aoff + m * 2048 + k * 1024); } while (0)
; #define G8_LDB(dst, b, h) do { _Pragma("unroll") for (int n = 0; n < 2; ++n) _Pragma("unroll") for (int k = 0; k < 2; ++k) dst[n][k] = *(const LAS bf16x8*)(lds + G8_SB(b, h) + boff + n * 2048 + k * 1024); } while (0)
; #define G8_MMA(ai, bj, At, Bt) do { __builtin_amdgcn_s_setprio(1); _Pragma("unroll") for (int m = 0; m < 4; ++m) _Pragma("unroll") for (int n = 0; n < 2; ++n) _Pragma("unroll") for (int k = 0; k < 2; ++k) \
;         acc[ai][bj][m][n] = __builtin_amdgcn_mfma_f32_16x16x32_bf16(Bt[n][k], At[m][k], acc[ai][bj][m][n], 0, 0, 0); __builtin_amdgcn_s_setprio(0); } while (0)
; #define G8_WAIT_V(n) asm volatile("s_waitcnt vmcnt(" #n ")" ::: "memory")
; #define G8_WAIT_L(n) asm volatile("s_waitcnt lgkmcnt(" #n ")" ::: "memory")
; #define G8_BAR __builtin_amdgcn_s_barrier()
; #define G8_SCHED __builtin_amdgcn_sched_barrier(0)
; template <class Epi, class Sched>
; __device__ __forceinline__ void gemm_phase(LAS unsigned char* lds, const int K, const Sched& S, const Epi& E) {
;     ...
;             G8_WAIT_V(6); G8_BAR; G8_MMA(1, 1, At, B1); G8_BAR;
;             G8_LDB(B0, 1, 0); G8_SCHED; G8_LDA(At, 1, 0); G8_STAGE(G8_SA(0, 1), a2, oc[1]);
;             G8_WAIT_L(8); G8_BAR; G8_WAIT_L(0); G8_MMA(0, 0, At, B0); G8_BAR; G8_SCHED;
;             G8_LDB(B1, 1, 1); G8_STAGE(G8_SB(1, 0), b3, voffB);
;             G8_BAR; G8_WAIT_L(0); G8_MMA(0, 1, At, B1); G8_BAR;
	v_mfma_f32_16x16x32_bf16 v[54:57], v[216:219], v[146:149], v[54:57]
	v_mfma_f32_16x16x32_bf16 v[50:53], v[224:227], v[146:149], v[50:53]
	v_mfma_f32_16x16x32_bf16 v[38:41], v[216:219], v[154:157], v[38:41]
	v_mfma_f32_16x16x32_bf16 v[34:37], v[224:227], v[154:157], v[34:37]
	v_mfma_f32_16x16x32_bf16 v[22:25], v[216:219], v[162:165], v[22:25]
	v_mfma_f32_16x16x32_bf16 v[18:21], v[224:227], v[162:165], v[18:21]
	v_mfma_f32_16x16x32_bf16 v[6:9], v[216:219], v[170:173], v[6:9]
	v_mfma_f32_16x16x32_bf16 v[2:5], v[224:227], v[170:173], v[2:5]
	v_mfma_f32_16x16x32_bf16 v[54:57], v[220:223], v[150:153], v[54:57]
	s_add_i32 s58, 0, 0x18000
	v_mfma_f32_16x16x32_bf16 v[50:53], v[228:231], v[150:153], v[50:53]
	v_add_u32_e32 v142, s58, v198
	v_mfma_f32_16x16x32_bf16 v[38:41], v[220:223], v[158:161], v[38:41]
	v_mfma_f32_16x16x32_bf16 v[34:37], v[228:231], v[158:161], v[34:37]
	v_mfma_f32_16x16x32_bf16 v[22:25], v[220:223], v[166:169], v[22:25]
	v_mfma_f32_16x16x32_bf16 v[18:21], v[228:231], v[166:169], v[18:21]
	v_mfma_f32_16x16x32_bf16 v[6:9], v[220:223], v[174:177], v[6:9]
	v_mfma_f32_16x16x32_bf16 v[2:5], v[228:231], v[174:177], v[2:5]
	s_setprio 0
	s_barrier
	ds_read_b128 v[130:133], v142
	ds_read_b128 v[134:137], v142 offset:1024
	ds_read_b128 v[138:141], v142 offset:2048
	ds_read_b128 v[142:145], v142 offset:3072
	s_mov_b32 m0, s46
	v_lshl_add_u64 v[190:191], s[34:35], 0, v[190:191]
	ds_read_b128 v[146:149], v200 offset:32768
	ds_read_b128 v[150:153], v200 offset:33792
	ds_read_b128 v[154:157], v200 offset:34816
	ds_read_b128 v[158:161], v200 offset:35840
	ds_read_b128 v[162:165], v200 offset:36864
	ds_read_b128 v[166:169], v200 offset:37888
	ds_read_b128 v[170:173], v200 offset:38912
	ds_read_b128 v[174:177], v200 offset:39936
	global_load_lds_dwordx4 v[190:191], off
	v_lshl_add_u64 v[190:191], s[34:35], 0, v[186:187]
	s_mov_b32 m0, s47
	s_nop 0
	global_load_lds_dwordx4 v[190:191], off
	s_waitcnt lgkmcnt(8)
	s_setprio 1
	s_barrier
	s_waitcnt lgkmcnt(0)
	v_mfma_f32_16x16x32_bf16 v[126:129], v[130:133], v[146:149], v[126:129]
	v_mfma_f32_16x16x32_bf16 v[122:125], v[138:141], v[146:149], v[122:125]
	v_mfma_f32_16x16x32_bf16 v[110:113], v[130:133], v[154:157], v[110:113]
	v_mfma_f32_16x16x32_bf16 v[106:109], v[138:141], v[154:157], v[106:109]
	v_mfma_f32_16x16x32_bf16 v[94:97], v[130:133], v[162:165], v[94:97]
	v_mfma_f32_16x16x32_bf16 v[90:93], v[138:141], v[162:165], v[90:93]
	v_mfma_f32_16x16x32_bf16 v[78:81], v[130:133], v[170:173], v[78:81]
	v_mfma_f32_16x16x32_bf16 v[74:77], v[138:141], v[170:173], v[74:77]
	v_mfma_f32_16x16x32_bf16 v[126:129], v[134:137], v[150:153], v[126:129]
	v_mfma_f32_16x16x32_bf16 v[122:125], v[142:145], v[150:153], v[122:125]
	v_mfma_f32_16x16x32_bf16 v[110:113], v[134:137], v[158:161], v[110:113]
	v_mfma_f32_16x16x32_bf16 v[106:109], v[142:145], v[158:161], v[106:109]
	v_mfma_f32_16x16x32_bf16 v[94:97], v[134:137], v[166:169], v[94:97]
	v_mfma_f32_16x16x32_bf16 v[90:93], v[142:145], v[166:169], v[90:93]
	v_mfma_f32_16x16x32_bf16 v[78:81], v[134:137], v[174:177], v[78:81]
	v_mfma_f32_16x16x32_bf16 v[74:77], v[142:145], v[174:177], v[74:77]
	s_setprio 0
	s_barrier
	s_add_i32 s34, 0, 0x1c000
	s_add_i32 s35, s58, s41
	v_add_u32_e32 v183, s34, v198
	v_lshl_add_u64 v[190:191], v[232:233], 0, s[18:19]
	s_mov_b32 m0, s35
	ds_read_b128 v[216:219], v183
	ds_read_b128 v[220:223], v183 offset:1024
	ds_read_b128 v[224:227], v183 offset:2048
	ds_read_b128 v[228:231], v183 offset:3072
	global_load_lds_dwordx4 v[190:191], off
	v_lshl_add_u64 v[190:191], v[234:235], 0, s[18:19]
	s_add_i32 m0, s35, 0x2000
	s_nop 0
	global_load_lds_dwordx4 v[190:191], off
	s_setprio 1
	s_barrier
; #define G8_STAGE(bufoff, gbase, voff) do { _Pragma("unroll") for (int _i = 0; _i < 2; ++_i) \
;         __builtin_amdgcn_global_load_lds((const unsigned*)((const char*)(gbase) + (voff)[_i]), (LAS unsigned*)(lds + (bufoff) + ldsw + _i * 8192), 16, 0, 0); } while (0)
; #define G8_LDA(dst, b, h) do { _Pragma("unroll") for (int m = 0; m < 4; ++m) _Pragma("unroll") for (int k = 0; k < 2; ++k) dst[m][k] = *(const LAS bf16x8*)(lds + G8_SA(b, h) + aoff + m * 2048 + k * 1024); } while (0)
; #define G8_MMA(ai, bj, At, Bt) do { __builtin_amdgcn_s_setprio(1); _Pragma("unroll") for (int m = 0; m < 4; ++m) _Pragma("unroll") for (int n = 0; n < 2; ++n) _Pragma("unroll") for (int k = 0; k < 2; ++k) \
;         acc[ai][bj][m][n] = __builtin_amdgcn_mfma_f32_16x16x32_bf16(Bt[n][k], At[m][k], acc[ai][bj][m][n], 0, 0, 0); __builtin_amdgcn_s_setprio(0); } while (0)
; #define G8_WAIT_V(n) asm volatile("s_waitcnt vmcnt(" #n ")" ::: "memory")
; #define G8_WAIT_L(n) asm volatile("s_waitcnt lgkmcnt(" #n ")" ::: "memory")
; #define G8_BAR __builtin_amdgcn_s_barrier()
; #define G8_SCHED __builtin_amdgcn_sched_barrier(0)
; template <class Epi, class Sched>
; __device__ __forceinline__ void gemm_phase(LAS unsigned char* lds, const int K, const Sched& S, const Epi& E) {
;     ...
;             G8_LDA(At, 1, 1); G8_STAGE(G8_SA(1, 0), a3, oc[0]);
;             G8_BAR; G8_WAIT_L(0); G8_MMA(1, 0, At, B0); G8_BAR; G8_SCHED;
;             G8_STAGE(G8_SB(1, 1), b3 + hstep, voffB);
;             G8_WAIT_V(6); G8_BAR; G8_MMA(1, 1, At, B1); G8_BAR;
;         }
	s_waitcnt lgkmcnt(0)
	v_mfma_f32_16x16x32_bf16 v[118:121], v[216:219], v[146:149], v[118:121]
	v_mfma_f32_16x16x32_bf16 v[114:117], v[224:227], v[146:149], v[114:117]
	v_mfma_f32_16x16x32_bf16 v[102:105], v[216:219], v[154:157], v[102:105]
	v_mfma_f32_16x16x32_bf16 v[98:101], v[224:227], v[154:157], v[98:101]
	v_mfma_f32_16x16x32_bf16 v[86:89], v[216:219], v[162:165], v[86:89]
	v_mfma_f32_16x16x32_bf16 v[82:85], v[224:227], v[162:165], v[82:85]
	v_mfma_f32_16x16x32_bf16 v[70:73], v[216:219], v[170:173], v[70:73]
	v_mfma_f32_16x16x32_bf16 v[66:69], v[224:227], v[170:173], v[66:69]
	v_mfma_f32_16x16x32_bf16 v[118:121], v[220:223], v[150:153], v[118:121]
	s_mov_b32 m0, s49
	v_mfma_f32_16x16x32_bf16 v[114:117], v[228:231], v[150:153], v[114:117]
	v_lshl_add_u64 v[190:191], v[236:237], 0, s[18:19]
	v_mfma_f32_16x16x32_bf16 v[102:105], v[220:223], v[158:161], v[102:105]
	v_mfma_f32_16x16x32_bf16 v[98:101], v[228:231], v[158:161], v[98:101]
	v_mfma_f32_16x16x32_bf16 v[86:89], v[220:223], v[166:169], v[86:89]
	v_mfma_f32_16x16x32_bf16 v[82:85], v[228:231], v[166:169], v[82:85]
	v_mfma_f32_16x16x32_bf16 v[70:73], v[220:223], v[174:177], v[70:73]
	v_mfma_f32_16x16x32_bf16 v[66:69], v[228:231], v[174:177], v[66:69]
	s_setprio 0
	s_barrier
	ds_read_b128 v[146:149], v200 offset:49152
	ds_read_b128 v[150:153], v200 offset:50176
	ds_read_b128 v[154:157], v200 offset:51200
	ds_read_b128 v[158:161], v200 offset:52224
	ds_read_b128 v[162:165], v200 offset:53248
	ds_read_b128 v[166:169], v200 offset:54272
	ds_read_b128 v[170:173], v200 offset:55296
	ds_read_b128 v[174:177], v200 offset:56320
	global_load_lds_dwordx4 v[190:191], off
	v_lshl_add_u64 v[190:191], v[238:239], 0, s[18:19]
	s_mov_b32 m0, s50
	s_nop 0
	global_load_lds_dwordx4 v[190:191], off
	s_setprio 1
	s_barrier
	s_waitcnt lgkmcnt(0)
	v_mfma_f32_16x16x32_bf16 v[62:65], v[130:133], v[146:149], v[62:65]
	v_mfma_f32_16x16x32_bf16 v[58:61], v[138:141], v[146:149], v[58:61]
	v_mfma_f32_16x16x32_bf16 v[46:49], v[130:133], v[154:157], v[46:49]
	v_mfma_f32_16x16x32_bf16 v[42:45], v[138:141], v[154:157], v[42:45]
	v_mfma_f32_16x16x32_bf16 v[30:33], v[130:133], v[162:165], v[30:33]
	v_mfma_f32_16x16x32_bf16 v[26:29], v[138:141], v[162:165], v[26:29]
	v_mfma_f32_16x16x32_bf16 v[14:17], v[130:133], v[170:173], v[14:17]
	v_mfma_f32_16x16x32_bf16 v[10:13], v[138:141], v[170:173], v[10:13]
	v_mfma_f32_16x16x32_bf16 v[62:65], v[134:137], v[150:153], v[62:65]
	v_mfma_f32_16x16x32_bf16 v[58:61], v[142:145], v[150:153], v[58:61]
	v_mfma_f32_16x16x32_bf16 v[46:49], v[134:137], v[158:161], v[46:49]
	v_mfma_f32_16x16x32_bf16 v[42:45], v[142:145], v[158:161], v[42:45]
	v_mfma_f32_16x16x32_bf16 v[30:33], v[134:137], v[166:169], v[30:33]
	v_mfma_f32_16x16x32_bf16 v[26:29], v[142:145], v[166:169], v[26:29]
	v_mfma_f32_16x16x32_bf16 v[14:17], v[134:137], v[174:177], v[14:17]
	v_mfma_f32_16x16x32_bf16 v[10:13], v[142:145], v[174:177], v[10:13]
	s_setprio 0
	s_barrier
	s_add_u32 s24, s24, 0x40080
	s_addc_u32 s25, s25, 0
	s_add_i32 s34, s34, s41
	v_lshl_add_u64 v[130:131], s[24:25], 0, v[178:179]
	s_mov_b32 m0, s34
	s_nop 0
	global_load_lds_dwordx4 v[130:131], off
	v_lshl_add_u64 v[130:131], s[24:25], 0, v[180:181]
	s_add_i32 m0, s34, 0x2000
	s_nop 0
	global_load_lds_dwordx4 v[130:131], off
	s_waitcnt vmcnt(6)
	s_setprio 1
	s_barrier
	v_mfma_f32_16x16x32_bf16 v[54:57], v[216:219], v[146:149], v[54:57]
	v_mfma_f32_16x16x32_bf16 v[50:53], v[224:227], v[146:149], v[50:53]
	v_mfma_f32_16x16x32_bf16 v[38:41], v[216:219], v[154:157], v[38:41]
	v_mfma_f32_16x16x32_bf16 v[34:37], v[224:227], v[154:157], v[34:37]
	v_mfma_f32_16x16x32_bf16 v[22:25], v[216:219], v[162:165], v[22:25]
	v_mfma_f32_16x16x32_bf16 v[18:21], v[224:227], v[162:165], v[18:21]
	v_mfma_f32_16x16x32_bf16 v[6:9], v[216:219], v[170:173], v[6:9]
	v_mfma_f32_16x16x32_bf16 v[2:5], v[224:227], v[170:173], v[2:5]
	v_mfma_f32_16x16x32_bf16 v[54:57], v[220:223], v[150:153], v[54:57]
	s_add_i32 s57, s57, 2
	v_mfma_f32_16x16x32_bf16 v[50:53], v[228:231], v[150:153], v[50:53]
	s_add_u32 s22, s22, 0x100
	v_mfma_f32_16x16x32_bf16 v[38:41], v[220:223], v[158:161], v[38:41]
	s_addc_u32 s23, s23, 0
	v_mfma_f32_16x16x32_bf16 v[34:37], v[228:231], v[158:161], v[34:37]
	s_add_u32 s55, s55, 0x100
	v_mfma_f32_16x16x32_bf16 v[22:25], v[220:223], v[166:169], v[22:25]
	s_addc_u32 s56, s56, 0
	v_mfma_f32_16x16x32_bf16 v[18:21], v[228:231], v[166:169], v[18:21]
	s_cmp_gt_u32 s57, 13
	v_mfma_f32_16x16x32_bf16 v[6:9], v[220:223], v[174:177], v[6:9]
	v_mfma_f32_16x16x32_bf16 v[2:5], v[228:231], v[174:177], v[2:5]
	s_setprio 0
	s_barrier
	s_cbranch_scc1 .LBB0_2529

; #define G8_STAGE(bufoff, gbase, voff) do { _Pragma("unroll") for (int _i = 0; _i < 2; ++_i) \
;         __builtin_amdgcn_global_load_lds((const unsigned*)((const char*)(gbase) + (voff)[_i]), (LAS unsigned*)(lds + (bufoff) + ldsw + _i * 8192), 16, 0, 0); } while (0)
; #define G8_LDA(dst, b, h) do { _Pragma("unroll") for (int m = 0; m < 4; ++m) _Pragma("unroll") for (int k = 0; k < 2; ++k) dst[m][k] = *(const LAS bf16x8*)(lds + G8_SA(b, h) + aoff + m * 2048 + k * 1024); } while (0)
; #define G8_LDB(dst, b, h) do { _Pragma("unroll") for (int n = 0; n < 2; ++n) _Pragma("unroll") for (int k = 0; k < 2; ++k) dst[n][k] = *(const LAS bf16x8*)(lds + G8_SB(b, h) + boff + n * 2048 + k * 1024); } while (0)
; #define G8_MMA(ai, bj, At, Bt) do { __builtin_amdgcn_s_setprio(1); _Pragma("unroll") for (int m = 0; m < 4; ++m) _Pragma("unroll") for (int n = 0; n < 2; ++n) _Pragma("unroll") for (int k = 0; k < 2; ++k) \
;         acc[ai][bj][m][n] = __builtin_amdgcn_mfma_f32_16x16x32_bf16(Bt[n][k], At[m][k], acc[ai][bj][m][n], 0, 0, 0); __builtin_amdgcn_s_setprio(0); } while (0)
; template <class Epi, class Sched>
; __device__ __forceinline__ void gemm_phase(LAS unsigned char* lds, const int K, const Sched& S, const Epi& E) {
;     ...
;         const bool has_next = S.next(ui + 1, nxt);
;         const char* nA = has_next ? nxt.A : cA; const char* nB = has_next ? nxt.B : cB;
; #pragma unroll 1
;         for (int t = 0; t < nt; t += 2) {
;             const bool last = (t == nt - 2);
;             const char* a1 = cA + (size_t)(t + 1) * kstep;
;             const char* a2 = last ? nA : cA + (size_t)(t + 2) * kstep; const char* b2 = last ? nB : cB + (size_t)(t + 2) * kstep;
;             const char* a3 = a2 + kstep; const char* b3 = b2 + kstep;
;             G8_LDB(B0, 0, 0); G8_SCHED; G8_LDA(At, 0, 0); G8_STAGE(G8_SA(1, 1), a1, oc[1]);
;             if (last && has_next) S.aoff(nxt, tid, oc);
;             G8_WAIT_L(8); G8_BAR; G8_WAIT_L(0); G8_MMA(0, 0, At, B0); G8_BAR; G8_SCHED;
;             G8_LDB(B1, 0, 1); G8_STAGE(G8_SB(0, 0), b2, voffB);
;             G8_BAR; G8_WAIT_L(0); G8_MMA(0, 1, At, B1); G8_BAR;
;             G8_LDA(At, 0, 1); G8_STAGE(G8_SA(0, 0), a2, oc[0]);
;             G8_BAR; G8_WAIT_L(0); G8_MMA(1, 0, At, B0); G8_BAR; G8_SCHED;
;             G8_STAGE(G8_SB(0, 1), b2 + hstep, voffB);
;             G8_WAIT_V(6); G8_BAR; G8_MMA(1, 1, At, B1); G8_BAR;
.LBB0_2616:
	s_xor_b64 s[40:41], s[42:43], -1
	s_add_u32 s44, s44, 0x100
	s_addc_u32 s45, s45, 0
	s_and_b64 s[42:43], s[36:37], exec
	s_cselect_b32 s43, s1, s45
	s_cselect_b32 s42, s0, s44
	s_add_u32 s38, s22, s38
	s_addc_u32 s39, s23, s39
	s_add_u32 s38, s38, 0x100
	s_addc_u32 s39, s39, 0
	s_and_b64 s[36:37], s[36:37], exec
	s_cselect_b32 s37, s35, s39
	s_cselect_b32 s36, s34, s38
	s_setprio 1
	s_waitcnt lgkmcnt(8)
	s_barrier
	s_waitcnt lgkmcnt(0)
	s_waitcnt lgkmcnt(0)
	v_mfma_f32_16x16x32_bf16 v[126:129], v[130:133], v[170:173], v[126:129]
	v_mfma_f32_16x16x32_bf16 v[122:125], v[138:141], v[170:173], v[122:125]
	v_mfma_f32_16x16x32_bf16 v[110:113], v[130:133], v[162:165], v[110:113]
	v_mfma_f32_16x16x32_bf16 v[106:109], v[138:141], v[162:165], v[106:109]
	v_mfma_f32_16x16x32_bf16 v[94:97], v[130:133], v[154:157], v[94:97]
	v_mfma_f32_16x16x32_bf16 v[90:93], v[138:141], v[154:157], v[90:93]
	v_mfma_f32_16x16x32_bf16 v[78:81], v[130:133], v[146:149], v[78:81]
	v_mfma_f32_16x16x32_bf16 v[74:77], v[138:141], v[146:149], v[74:77]
	v_mfma_f32_16x16x32_bf16 v[126:129], v[134:137], v[174:177], v[126:129]
	v_mfma_f32_16x16x32_bf16 v[122:125], v[142:145], v[174:177], v[122:125]
	v_mfma_f32_16x16x32_bf16 v[110:113], v[134:137], v[166:169], v[110:113]
	v_mfma_f32_16x16x32_bf16 v[106:109], v[142:145], v[166:169], v[106:109]
	v_mfma_f32_16x16x32_bf16 v[94:97], v[134:137], v[158:161], v[94:97]
	v_mfma_f32_16x16x32_bf16 v[90:93], v[142:145], v[158:161], v[90:93]
	v_mfma_f32_16x16x32_bf16 v[78:81], v[134:137], v[150:153], v[78:81]
	v_mfma_f32_16x16x32_bf16 v[74:77], v[142:145], v[150:153], v[74:77]
	s_setprio 0
	s_barrier
	s_add_i32 s44, 0, 0x14000
	s_mov_b32 m0, s52
	v_add_u32_e32 v183, s44, v200
	v_lshl_add_u64 v[236:237], s[36:37], 0, v[178:179]
	ds_read_b128 v[220:223], v183
	ds_read_b128 v[224:227], v183 offset:1024
	ds_read_b128 v[228:231], v183 offset:2048
	ds_read_b128 v[232:235], v183 offset:3072
	global_load_lds_dwordx4 v[236:237], off
	v_lshl_add_u64 v[238:239], s[36:37], 0, v[180:181]
	s_mov_b32 m0, s53
	s_nop 0
	global_load_lds_dwordx4 v[238:239], off
	s_setprio 1
	s_barrier
	s_waitcnt lgkmcnt(0)
	v_mfma_f32_16x16x32_bf16 v[118:121], v[220:223], v[170:173], v[118:121]
	v_mfma_f32_16x16x32_bf16 v[114:117], v[228:231], v[170:173], v[114:117]
	v_mfma_f32_16x16x32_bf16 v[102:105], v[220:223], v[162:165], v[102:105]
	v_mfma_f32_16x16x32_bf16 v[98:101], v[228:231], v[162:165], v[98:101]
	v_mfma_f32_16x16x32_bf16 v[86:89], v[220:223], v[154:157], v[86:89]
	v_mfma_f32_16x16x32_bf16 v[82:85], v[228:231], v[154:157], v[82:85]
	v_mfma_f32_16x16x32_bf16 v[70:73], v[220:223], v[146:149], v[70:73]
	v_mfma_f32_16x16x32_bf16 v[66:69], v[228:231], v[146:149], v[66:69]
	v_mfma_f32_16x16x32_bf16 v[118:121], v[224:227], v[174:177], v[118:121]
	s_mov_b32 m0, s51
	v_mfma_f32_16x16x32_bf16 v[114:117], v[232:235], v[174:177], v[114:117]
	v_mfma_f32_16x16x32_bf16 v[102:105], v[224:227], v[166:169], v[102:105]
	v_mfma_f32_16x16x32_bf16 v[98:101], v[232:235], v[166:169], v[98:101]
	v_mfma_f32_16x16x32_bf16 v[86:89], v[224:227], v[158:161], v[86:89]
	v_mfma_f32_16x16x32_bf16 v[82:85], v[232:235], v[158:161], v[82:85]
	v_mfma_f32_16x16x32_bf16 v[70:73], v[224:227], v[150:153], v[70:73]
	v_mfma_f32_16x16x32_bf16 v[66:69], v[232:235], v[150:153], v[66:69]
	s_setprio 0
	s_barrier
	ds_read_b128 v[146:149], v216 offset:16384
	ds_read_b128 v[150:153], v216 offset:17408
	ds_read_b128 v[154:157], v216 offset:18432
	ds_read_b128 v[158:161], v216 offset:19456
	ds_read_b128 v[162:165], v216 offset:20480
	ds_read_b128 v[166:169], v216 offset:21504
	ds_read_b128 v[170:173], v216 offset:22528
	ds_read_b128 v[174:177], v216 offset:23552
	global_load_lds_dwordx4 v182, s[42:43]
	s_mov_b32 m0, s54
	v_mov_b32_e32 v183, v1
	global_load_lds_dwordx4 v184, s[42:43]
	s_setprio 1
	s_barrier
	s_waitcnt lgkmcnt(0)
	v_mov_b32_e32 v185, v1
	v_lshl_add_u64 v[240:241], s[42:43], 0, v[182:183]
	v_lshl_add_u64 v[242:243], s[42:43], 0, v[184:185]
	s_waitcnt lgkmcnt(0)
	v_mfma_f32_16x16x32_bf16 v[62:65], v[130:133], v[146:149], v[62:65]
	v_mfma_f32_16x16x32_bf16 v[58:61], v[138:141], v[146:149], v[58:61]
	v_mfma_f32_16x16x32_bf16 v[46:49], v[130:133], v[154:157], v[46:49]
	v_mfma_f32_16x16x32_bf16 v[42:45], v[138:141], v[154:157], v[42:45]
	v_mfma_f32_16x16x32_bf16 v[30:33], v[130:133], v[162:165], v[30:33]
	v_mfma_f32_16x16x32_bf16 v[26:29], v[138:141], v[162:165], v[26:29]
	v_mfma_f32_16x16x32_bf16 v[14:17], v[130:133], v[170:173], v[14:17]
	v_mfma_f32_16x16x32_bf16 v[10:13], v[138:141], v[170:173], v[10:13]
	v_mfma_f32_16x16x32_bf16 v[62:65], v[134:137], v[150:153], v[62:65]
	v_mfma_f32_16x16x32_bf16 v[58:61], v[142:145], v[150:153], v[58:61]
	v_mfma_f32_16x16x32_bf16 v[46:49], v[134:137], v[158:161], v[46:49]
	v_mfma_f32_16x16x32_bf16 v[42:45], v[142:145], v[158:161], v[42:45]
	v_mfma_f32_16x16x32_bf16 v[30:33], v[134:137], v[166:169], v[30:33]
	v_mfma_f32_16x16x32_bf16 v[26:29], v[142:145], v[166:169], v[26:29]
	v_mfma_f32_16x16x32_bf16 v[14:17], v[134:137], v[174:177], v[14:17]
	v_mfma_f32_16x16x32_bf16 v[10:13], v[142:145], v[174:177], v[10:13]
	s_setprio 0
	s_barrier
	s_add_u32 s38, s36, 0x10000
	s_addc_u32 s39, s37, 0
	s_add_i32 s44, s44, s50
	v_lshl_add_u64 v[130:131], s[38:39], 0, v[178:179]
	s_mov_b32 m0, s44
	s_nop 0
	global_load_lds_dwordx4 v[130:131], off
	v_lshl_add_u64 v[130:131], s[38:39], 0, v[180:181]
	s_add_i32 m0, s44, 0x2000
	s_nop 0
	global_load_lds_dwordx4 v[130:131], off
	s_waitcnt vmcnt(6)
	s_setprio 1
	s_barrier
; #define G8_STAGE(bufoff, gbase, voff) do { _Pragma("unroll") for (int _i = 0; _i < 2; ++_i) \
;         __builtin_amdgcn_global_load_lds((const unsigned*)((const char*)(gbase) + (voff)[_i]), (LAS unsigned*)(lds + (bufoff) + ldsw + _i * 8192), 16, 0, 0); } while (0)
; #define G8_LDA(dst, b, h) do { _Pragma("unroll") for (int m = 0; m < 4; ++m) _Pragma("unroll") for (int k = 0; k < 2; ++k) dst[m][k] = *(const LAS bf16x8*)(lds + G8_SA(b, h) + aoff + m * 2048 + k * 1024); } while (0)
; #define G8_LDB(dst, b, h) do { _Pragma("unroll") for (int n = 0; n < 2; ++n) _Pragma("unroll") for (int k = 0; k < 2; ++k) dst[n][k] = *(const LAS bf16x8*)(lds + G8_SB(b, h) + boff + n * 2048 + k * 1024); } while (0)
; #define G8_MMA(ai, bj, At, Bt) do { __builtin_amdgcn_s_setprio(1); _Pragma("unroll") for (int m = 0; m < 4; ++m) _Pragma("unroll") for (int n = 0; n < 2; ++n) _Pragma("unroll") for (int k = 0; k < 2; ++k) \
;         acc[ai][bj][m][n] = __builtin_amdgcn_mfma_f32_16x16x32_bf16(Bt[n][k], At[m][k], acc[ai][bj][m][n], 0, 0, 0); __builtin_amdgcn_s_setprio(0); } while (0)
; #define G8_WAIT_V(n) asm volatile("s_waitcnt vmcnt(" #n ")" ::: "memory")
; #define G8_WAIT_L(n) asm volatile("s_waitcnt lgkmcnt(" #n ")" ::: "memory")
; #define G8_BAR __builtin_amdgcn_s_barrier()
; #define G8_SCHED __builtin_amdgcn_sched_barrier(0)
; template <class Epi, class Sched>
; __device__ __forceinline__ void gemm_phase(LAS unsigned char* lds, const int K, const Sched& S, const Epi& E) {
;     ...
;             G8_WAIT_V(6); G8_BAR; G8_MMA(1, 1, At, B1); G8_BAR;
;             G8_LDB(B0, 1, 0); G8_SCHED; G8_LDA(At, 1, 0); G8_STAGE(G8_SA(0, 1), a2, oc[1]);
;             G8_WAIT_L(8); G8_BAR; G8_WAIT_L(0); G8_MMA(0, 0, At, B0); G8_BAR; G8_SCHED;
;             G8_LDB(B1, 1, 1); G8_STAGE(G8_SB(1, 0), b3, voffB);
;             G8_BAR; G8_WAIT_L(0); G8_MMA(0, 1, At, B1); G8_BAR;
	v_mfma_f32_16x16x32_bf16 v[54:57], v[220:223], v[146:149], v[54:57]
	v_mfma_f32_16x16x32_bf16 v[50:53], v[228:231], v[146:149], v[50:53]
	v_mfma_f32_16x16x32_bf16 v[38:41], v[220:223], v[154:157], v[38:41]
	v_mfma_f32_16x16x32_bf16 v[34:37], v[228:231], v[154:157], v[34:37]
	v_mfma_f32_16x16x32_bf16 v[22:25], v[220:223], v[162:165], v[22:25]
	v_mfma_f32_16x16x32_bf16 v[18:21], v[228:231], v[162:165], v[18:21]
	v_mfma_f32_16x16x32_bf16 v[6:9], v[220:223], v[170:173], v[6:9]
	v_mfma_f32_16x16x32_bf16 v[2:5], v[228:231], v[170:173], v[2:5]
	v_mfma_f32_16x16x32_bf16 v[54:57], v[224:227], v[150:153], v[54:57]
	s_add_i32 s38, 0, 0x18000
	v_mfma_f32_16x16x32_bf16 v[50:53], v[232:235], v[150:153], v[50:53]
	v_add_u32_e32 v142, s38, v200
	v_mfma_f32_16x16x32_bf16 v[38:41], v[224:227], v[158:161], v[38:41]
	v_mfma_f32_16x16x32_bf16 v[34:37], v[232:235], v[158:161], v[34:37]
	v_mfma_f32_16x16x32_bf16 v[22:25], v[224:227], v[166:169], v[22:25]
	v_mfma_f32_16x16x32_bf16 v[18:21], v[232:235], v[166:169], v[18:21]
	v_mfma_f32_16x16x32_bf16 v[6:9], v[224:227], v[174:177], v[6:9]
	v_mfma_f32_16x16x32_bf16 v[2:5], v[232:235], v[174:177], v[2:5]
	s_setprio 0
	s_barrier
	ds_read_b128 v[130:133], v142
	ds_read_b128 v[134:137], v142 offset:1024
	ds_read_b128 v[138:141], v142 offset:2048
	ds_read_b128 v[142:145], v142 offset:3072
	s_mov_b32 m0, s55
	v_lshl_add_u64 v[220:221], s[42:43], 0, v[0:1]
	ds_read_b128 v[146:149], v216 offset:32768
	ds_read_b128 v[150:153], v216 offset:33792
	ds_read_b128 v[154:157], v216 offset:34816
	ds_read_b128 v[158:161], v216 offset:35840
	ds_read_b128 v[162:165], v216 offset:36864
	ds_read_b128 v[166:169], v216 offset:37888
	ds_read_b128 v[170:173], v216 offset:38912
	ds_read_b128 v[174:177], v216 offset:39936
	global_load_lds_dwordx4 v[220:221], off
	v_lshl_add_u64 v[220:221], s[42:43], 0, v[186:187]
	s_mov_b32 m0, s56
	s_nop 0
	global_load_lds_dwordx4 v[220:221], off
	s_waitcnt lgkmcnt(8)
	s_setprio 1
	s_barrier
	s_waitcnt lgkmcnt(0)
	v_mfma_f32_16x16x32_bf16 v[126:129], v[130:133], v[146:149], v[126:129]
	v_mfma_f32_16x16x32_bf16 v[122:125], v[138:141], v[146:149], v[122:125]
	v_mfma_f32_16x16x32_bf16 v[110:113], v[130:133], v[154:157], v[110:113]
	v_mfma_f32_16x16x32_bf16 v[106:109], v[138:141], v[154:157], v[106:109]
	v_mfma_f32_16x16x32_bf16 v[94:97], v[130:133], v[162:165], v[94:97]
	v_mfma_f32_16x16x32_bf16 v[90:93], v[138:141], v[162:165], v[90:93]
	v_mfma_f32_16x16x32_bf16 v[78:81], v[130:133], v[170:173], v[78:81]
	v_mfma_f32_16x16x32_bf16 v[74:77], v[138:141], v[170:173], v[74:77]
	v_mfma_f32_16x16x32_bf16 v[126:129], v[134:137], v[150:153], v[126:129]
	v_mfma_f32_16x16x32_bf16 v[122:125], v[142:145], v[150:153], v[122:125]
	v_mfma_f32_16x16x32_bf16 v[110:113], v[134:137], v[158:161], v[110:113]
	v_mfma_f32_16x16x32_bf16 v[106:109], v[142:145], v[158:161], v[106:109]
	v_mfma_f32_16x16x32_bf16 v[94:97], v[134:137], v[166:169], v[94:97]
	v_mfma_f32_16x16x32_bf16 v[90:93], v[142:145], v[166:169], v[90:93]
	v_mfma_f32_16x16x32_bf16 v[78:81], v[134:137], v[174:177], v[78:81]
	v_mfma_f32_16x16x32_bf16 v[74:77], v[142:145], v[174:177], v[74:77]
	s_setprio 0
	s_barrier
	s_add_i32 s39, 0, 0x1c000
	s_add_i32 s38, s38, s50
	v_add_u32_e32 v183, s39, v200
	v_lshl_add_u64 v[236:237], v[236:237], 0, s[18:19]
	s_mov_b32 m0, s38
	ds_read_b128 v[220:223], v183
	ds_read_b128 v[224:227], v183 offset:1024
	ds_read_b128 v[228:231], v183 offset:2048
	ds_read_b128 v[232:235], v183 offset:3072
	global_load_lds_dwordx4 v[236:237], off
	v_lshl_add_u64 v[236:237], v[238:239], 0, s[18:19]
	s_add_i32 m0, s38, 0x2000
	s_nop 0
	global_load_lds_dwordx4 v[236:237], off
	s_setprio 1
	s_barrier
; #define G8_STAGE(bufoff, gbase, voff) do { _Pragma("unroll") for (int _i = 0; _i < 2; ++_i) \
;         __builtin_amdgcn_global_load_lds((const unsigned*)((const char*)(gbase) + (voff)[_i]), (LAS unsigned*)(lds + (bufoff) + ldsw + _i * 8192), 16, 0, 0); } while (0)
; #define G8_LDA(dst, b, h) do { _Pragma("unroll") for (int m = 0; m < 4; ++m) _Pragma("unroll") for (int k = 0; k < 2; ++k) dst[m][k] = *(const LAS bf16x8*)(lds + G8_SA(b, h) + aoff + m * 2048 + k * 1024); } while (0)
; #define G8_MMA(ai, bj, At, Bt) do { __builtin_amdgcn_s_setprio(1); _Pragma("unroll") for (int m = 0; m < 4; ++m) _Pragma("unroll") for (int n = 0; n < 2; ++n) _Pragma("unroll") for (int k = 0; k < 2; ++k) \
;         acc[ai][bj][m][n] = __builtin_amdgcn_mfma_f32_16x16x32_bf16(Bt[n][k], At[m][k], acc[ai][bj][m][n], 0, 0, 0); __builtin_amdgcn_s_setprio(0); } while (0)
; #define G8_WAIT_V(n) asm volatile("s_waitcnt vmcnt(" #n ")" ::: "memory")
; #define G8_WAIT_L(n) asm volatile("s_waitcnt lgkmcnt(" #n ")" ::: "memory")
; #define G8_BAR __builtin_amdgcn_s_barrier()
; #define G8_SCHED __builtin_amdgcn_sched_barrier(0)
; template <class Epi, class Sched>
; __device__ __forceinline__ void gemm_phase(LAS unsigned char* lds, const int K, const Sched& S, const Epi& E) {
;     ...
;             G8_LDA(At, 1, 1); G8_STAGE(G8_SA(1, 0), a3, oc[0]);
;             G8_BAR; G8_WAIT_L(0); G8_MMA(1, 0, At, B0); G8_BAR; G8_SCHED;
;             G8_STAGE(G8_SB(1, 1), b3 + hstep, voffB);
;             G8_WAIT_V(6); G8_BAR; G8_MMA(1, 1, At, B1); G8_BAR;
;         }
	s_waitcnt lgkmcnt(0)
	v_mfma_f32_16x16x32_bf16 v[118:121], v[220:223], v[146:149], v[118:121]
	v_mfma_f32_16x16x32_bf16 v[114:117], v[228:231], v[146:149], v[114:117]
	v_mfma_f32_16x16x32_bf16 v[102:105], v[220:223], v[154:157], v[102:105]
	v_mfma_f32_16x16x32_bf16 v[98:101], v[228:231], v[154:157], v[98:101]
	v_mfma_f32_16x16x32_bf16 v[86:89], v[220:223], v[162:165], v[86:89]
	v_mfma_f32_16x16x32_bf16 v[82:85], v[228:231], v[162:165], v[82:85]
	v_mfma_f32_16x16x32_bf16 v[70:73], v[220:223], v[170:173], v[70:73]
	v_mfma_f32_16x16x32_bf16 v[66:69], v[228:231], v[170:173], v[66:69]
	v_mfma_f32_16x16x32_bf16 v[118:121], v[224:227], v[150:153], v[118:121]
	s_mov_b32 m0, s57
	v_mfma_f32_16x16x32_bf16 v[114:117], v[232:235], v[150:153], v[114:117]
	v_lshl_add_u64 v[236:237], v[240:241], 0, s[18:19]
	v_mfma_f32_16x16x32_bf16 v[102:105], v[224:227], v[158:161], v[102:105]
	v_mfma_f32_16x16x32_bf16 v[98:101], v[232:235], v[158:161], v[98:101]
	v_mfma_f32_16x16x32_bf16 v[86:89], v[224:227], v[166:169], v[86:89]
	v_mfma_f32_16x16x32_bf16 v[82:85], v[232:235], v[166:169], v[82:85]
	v_mfma_f32_16x16x32_bf16 v[70:73], v[224:227], v[174:177], v[70:73]
	v_mfma_f32_16x16x32_bf16 v[66:69], v[232:235], v[174:177], v[66:69]
	s_setprio 0
	s_barrier
	ds_read_b128 v[146:149], v216 offset:49152
	ds_read_b128 v[150:153], v216 offset:50176
	ds_read_b128 v[154:157], v216 offset:51200
	ds_read_b128 v[158:161], v216 offset:52224
	ds_read_b128 v[162:165], v216 offset:53248
	ds_read_b128 v[166:169], v216 offset:54272
	ds_read_b128 v[170:173], v216 offset:55296
	ds_read_b128 v[174:177], v216 offset:56320
	global_load_lds_dwordx4 v[236:237], off
	v_lshl_add_u64 v[236:237], v[242:243], 0, s[18:19]
	s_mov_b32 m0, s58
	s_nop 0
	global_load_lds_dwordx4 v[236:237], off
	s_setprio 1
	s_barrier
	s_waitcnt lgkmcnt(0)
	v_mfma_f32_16x16x32_bf16 v[62:65], v[130:133], v[146:149], v[62:65]
	v_mfma_f32_16x16x32_bf16 v[58:61], v[138:141], v[146:149], v[58:61]
	v_mfma_f32_16x16x32_bf16 v[46:49], v[130:133], v[154:157], v[46:49]
	v_mfma_f32_16x16x32_bf16 v[42:45], v[138:141], v[154:157], v[42:45]
	v_mfma_f32_16x16x32_bf16 v[30:33], v[130:133], v[162:165], v[30:33]
	v_mfma_f32_16x16x32_bf16 v[26:29], v[138:141], v[162:165], v[26:29]
	v_mfma_f32_16x16x32_bf16 v[14:17], v[130:133], v[170:173], v[14:17]
	v_mfma_f32_16x16x32_bf16 v[10:13], v[138:141], v[170:173], v[10:13]
	v_mfma_f32_16x16x32_bf16 v[62:65], v[134:137], v[150:153], v[62:65]
	v_mfma_f32_16x16x32_bf16 v[58:61], v[142:145], v[150:153], v[58:61]
	v_mfma_f32_16x16x32_bf16 v[46:49], v[134:137], v[158:161], v[46:49]
	v_mfma_f32_16x16x32_bf16 v[42:45], v[142:145], v[158:161], v[42:45]
	v_mfma_f32_16x16x32_bf16 v[30:33], v[134:137], v[166:169], v[30:33]
	v_mfma_f32_16x16x32_bf16 v[26:29], v[142:145], v[166:169], v[26:29]
	v_mfma_f32_16x16x32_bf16 v[14:17], v[134:137], v[174:177], v[14:17]
	v_mfma_f32_16x16x32_bf16 v[10:13], v[142:145], v[174:177], v[10:13]
	s_setprio 0
	s_barrier
	s_add_u32 s36, s36, 0x10080
	s_addc_u32 s37, s37, 0
	s_add_i32 s38, s39, s50
	v_lshl_add_u64 v[130:131], s[36:37], 0, v[178:179]
	s_mov_b32 m0, s38
	s_nop 0
	global_load_lds_dwordx4 v[130:131], off
	v_lshl_add_u64 v[130:131], s[36:37], 0, v[180:181]
	s_add_i32 m0, s38, 0x2000
	s_nop 0
	global_load_lds_dwordx4 v[130:131], off
	s_waitcnt vmcnt(6)
	s_setprio 1
	s_barrier
	v_mfma_f32_16x16x32_bf16 v[54:57], v[220:223], v[146:149], v[54:57]
	v_mfma_f32_16x16x32_bf16 v[50:53], v[228:231], v[146:149], v[50:53]
	v_mfma_f32_16x16x32_bf16 v[38:41], v[220:223], v[154:157], v[38:41]
	v_mfma_f32_16x16x32_bf16 v[34:37], v[228:231], v[154:157], v[34:37]
	v_mfma_f32_16x16x32_bf16 v[22:25], v[220:223], v[162:165], v[22:25]
	v_mfma_f32_16x16x32_bf16 v[18:21], v[228:231], v[162:165], v[18:21]
	v_mfma_f32_16x16x32_bf16 v[6:9], v[220:223], v[170:173], v[6:9]
	v_mfma_f32_16x16x32_bf16 v[2:5], v[228:231], v[170:173], v[2:5]
	v_mfma_f32_16x16x32_bf16 v[54:57], v[224:227], v[150:153], v[54:57]
	v_mfma_f32_16x16x32_bf16 v[50:53], v[232:235], v[150:153], v[50:53]
	v_mfma_f32_16x16x32_bf16 v[38:41], v[224:227], v[158:161], v[38:41]
	v_mfma_f32_16x16x32_bf16 v[34:37], v[232:235], v[158:161], v[34:37]
	v_mfma_f32_16x16x32_bf16 v[22:25], v[224:227], v[166:169], v[22:25]
	v_mfma_f32_16x16x32_bf16 v[18:21], v[232:235], v[166:169], v[18:21]
	v_mfma_f32_16x16x32_bf16 v[6:9], v[224:227], v[174:177], v[6:9]
	v_mfma_f32_16x16x32_bf16 v[2:5], v[232:235], v[174:177], v[2:5]
	s_setprio 0
	s_mov_b64 s[42:43], 0
	s_mov_b64 s[36:37], -1
	s_and_b64 vcc, exec, s[40:41]
	s_barrier
	s_cbranch_vccnz .LBB0_2618
	s_mov_b64 s[38:39], 0x100
	s_branch .LBB0_2614
	s_nop 0
	s_nop 0
	s_nop 0
	s_nop 0
